# speedup vs baseline: 1.0068x; 1.0041x over previous
.LBB3_11:
	v_lshl_or_b32 v64, s46, 8, v134
	v_lshl_add_u32 v68, s45, 7, v132
	v_ashrrev_i32_e32 v65, 31, v64
	s_waitcnt lgkmcnt(0)
	v_mad_i64_i32 v[66:67], s[22:23], v68, s44, 0
	v_lshl_add_u64 v[66:67], v[66:67], 2, s[14:15]
	v_lshlrev_b64 v[64:65], 2, v[64:65]
	v_lshl_add_u64 v[66:67], v[66:67], 0, v[64:65]
	global_store_dwordx4 v[66:67], v[60:63], off sc0 sc1
	global_store_dwordx4 v[66:67], v[56:59], off offset:64 sc0 sc1
	global_store_dwordx4 v[66:67], v[52:55], off offset:512 sc0 sc1
	global_store_dwordx4 v[66:67], v[48:51], off offset:576 sc0 sc1
	s_cmp_eq_u32 s4, s43
	s_mov_b64 s[24:25], s[20:21]
	v_or_b32_e32 v48, 16, v68
	v_mad_i64_i32 v[48:49], s[22:23], v48, s44, 0
	v_lshl_add_u64 v[48:49], v[48:49], 2, s[14:15]
	v_lshl_add_u64 v[48:49], v[48:49], 0, v[64:65]
	global_store_dwordx4 v[48:49], v[44:47], off sc0 sc1
	global_store_dwordx4 v[48:49], v[40:43], off offset:64 sc0 sc1
	global_store_dwordx4 v[48:49], v[36:39], off offset:512 sc0 sc1
	global_store_dwordx4 v[48:49], v[32:35], off offset:576 sc0 sc1
	s_mov_b32 s45, s50
	s_mov_b32 s46, s49
	v_or_b32_e32 v32, 32, v68
	v_mad_i64_i32 v[32:33], s[22:23], v32, s44, 0
	v_lshl_add_u64 v[32:33], v[32:33], 2, s[14:15]
	v_lshl_add_u64 v[32:33], v[32:33], 0, v[64:65]
	global_store_dwordx4 v[32:33], v[28:31], off sc0 sc1
	global_store_dwordx4 v[32:33], v[24:27], off offset:64 sc0 sc1
	global_store_dwordx4 v[32:33], v[20:23], off offset:512 sc0 sc1
	global_store_dwordx4 v[32:33], v[16:19], off offset:576 sc0 sc1
	s_nop 1
	v_or_b32_e32 v16, 48, v68
	v_mad_i64_i32 v[16:17], s[22:23], v16, s44, 0
	v_lshl_add_u64 v[16:17], v[16:17], 2, s[14:15]
	v_lshl_add_u64 v[16:17], v[16:17], 0, v[64:65]
	s_mov_b64 s[22:23], s[18:19]
	global_store_dwordx4 v[16:17], v[12:15], off sc0 sc1
	global_store_dwordx4 v[16:17], v[8:11], off offset:64 sc0 sc1
	global_store_dwordx4 v[16:17], v[4:7], off offset:512 sc0 sc1
	global_store_dwordx4 v[16:17], v[0:3], off offset:576 sc0 sc1
	s_cbranch_scc1 .LBB3_27
